# code placement: P1 fp8 projection K-loop (and its epilogue) moved by +32 bytes with unreachable padding, all later K-loops kept at the same address modulo 64
# baseline (speedup 1.0000x reference)
.LBB0_340:
	s_mov_b64 s[42:43], 0x80
	s_add_i32 m0, s83, 0x18000
	v_lshl_add_u64 v[6:7], v[6:7], 0, s[42:43]
	s_waitcnt vmcnt(2)
	s_barrier
	global_load_lds_dwordx4 v[6:7], off
	v_lshl_add_u64 v[4:5], v[4:5], 0, s[42:43]
	s_add_i32 m0, s83, 0x1a000
	s_add_i32 s87, s83, 0x8000
	s_add_i32 s88, s83, 0xa000
	global_load_lds_dwordx4 v[4:5], off
	v_lshl_add_u64 v[0:1], v[0:1], 0, s[42:43]
	s_mov_b32 m0, s87
	s_add_u32 s10, s8, 0x40080
	global_load_lds_dwordx4 v[0:1], off
	v_lshl_add_u64 v[0:1], v[2:3], 0, s[42:43]
	s_mov_b32 m0, s88
	s_addc_u32 s11, s9, 0
	global_load_lds_dwordx4 v[0:1], off
	s_add_i32 m0, s83, 0x1c000
	v_lshl_add_u64 v[0:1], s[10:11], 0, v[162:163]
	global_load_lds_dwordx4 v[0:1], off
	v_lshl_add_u64 v[0:1], s[10:11], 0, v[166:167]
	s_add_i32 m0, s83, 0x1e000
	s_waitcnt vmcnt(0)
	v_and_b32_e32 v16, 15, v8
	global_load_lds_dwordx4 v[0:1], off
	v_lshlrev_b32_e32 v0, 14, v9
	v_and_b32_e32 v0, 0xffff8000, v0
	v_lshl_add_u32 v0, v10, 11, v0
	v_and_b32_e32 v1, 1, v9
	v_or_b32_e32 v17, s39, v16
	v_lshl_or_b32 v0, v1, 6, v0
	v_lshlrev_b32_e32 v18, 6, v17
	v_and_b32_e32 v19, 48, v8
	s_movk_i32 s5, 0x3c0
	v_lshl_add_u32 v170, v11, 1, v0
	v_lshlrev_b32_e32 v0, 14, v12
	v_and_or_b32 v18, v18, s5, v19
	v_readlane_b32 s5, v251, 16
	v_and_b32_e32 v0, 0xffff8000, v0
	v_and_b32_e32 v15, 0xfffffc00, v15
	v_lshlrev_b32_e32 v17, 2, v17
	v_lshlrev_b32_e32 v8, 2, v8
	s_cmpk_lt_u32 s5, 0x100
	v_lshl_add_u32 v0, v13, 11, v0
	v_and_b32_e32 v1, 1, v12
	v_add_u32_e32 v20, s63, v15
	v_and_b32_e32 v17, 32, v17
	v_lshl_or_b32 v16, v16, 6, v19
	v_add_u32_e32 v15, s65, v15
	v_and_b32_e32 v8, 32, v8
	s_waitcnt vmcnt(6)
	s_cselect_b64 s[44:45], -1, 0
	s_cmp_eq_u32 s61, 0
	v_lshl_or_b32 v0, v1, 6, v0
	v_bitop3_b32 v17, v18, v20, v17 bitop3:0xde
	v_bitop3_b32 v182, v16, v15, v8 bitop3:0xde
	s_cselect_b64 s[46:47], -1, 0
	v_lshl_add_u32 v172, v14, 1, v0
	s_add_i32 s89, 0, 0x10000
	s_add_i32 s90, 0, 0x14000
	v_mbcnt_lo_u32_b32 v0, -1, 0
	v_mov_b32_e32 v171, v169
	v_mov_b32_e32 v173, v169
	v_add_u32_e32 v183, s89, v182
	v_add_u32_e32 v184, s90, v182
	v_add_u32_e32 v185, 0, v17
	s_mov_b32 s48, 0x39000000
	s_mov_b32 s50, 0x3e6d3388
	s_mov_b32 s52, 0x3f07dc22
	s_mov_b32 s54, 0xbf3a00e3
	s_mov_b32 s56, 0x3f35f0e3
	s_mov_b32 s58, 0xbe11a98e
	s_mov_b32 s60, 0x3e027906
	s_mov_b32 s62, 0xbf38aa3b
	s_mov_b32 s64, 0xb938aa3b
	v_mbcnt_hi_u32_b32 v186, -1, v0
	s_barrier
	s_branch .LBB0_343
	s_nop 0
	s_nop 0
	s_nop 0
	s_nop 0
	s_nop 0
	s_nop 0
	s_nop 0
	s_nop 0

.LBB0_491:
	s_nop 0
	s_nop 0
	s_nop 0
	s_nop 0
	s_nop 0
	s_nop 0
	s_nop 0
	s_nop 0
	v_readlane_b32 s4, v251, 10
	v_readlane_b32 s6, v251, 12
	v_readlane_b32 s7, v251, 13
	s_add_u32 s30, s6, 0x100000
	s_addc_u32 s31, s7, 0
	v_readlane_b32 s5, v251, 11
	s_add_u32 s36, s6, 0x4100000
	v_readlane_b32 s0, v251, 0
	s_addc_u32 s37, s7, 0
	s_not_b32 s0, s0
	v_readlane_b32 s4, v251, 19
	s_add_i32 s47, s4, s0
	v_readlane_b32 s1, v251, 1
	s_cmpk_lt_i32 s47, 0x200
	s_cselect_b64 s[0:1], -1, 0
	s_cmpk_gt_i32 s47, 0x1ff
	v_readlane_b32 s5, v251, 20
	v_mbcnt_lo_u32_b32 v8, -1, 0
	v_mbcnt_hi_u32_b32 v8, -1, v8
	s_cbranch_scc1 .LBB0_494
	s_ashr_i32 s4, s47, 31
	s_lshr_b32 s4, s4, 29
	s_add_i32 s8, s47, s4
	s_and_b32 s4, s8, -8
	s_sub_i32 s6, s47, s4
	s_cmp_gt_i32 s6, -1
	s_cbranch_scc0 .LBB0_495
	s_lshl_b32 s7, s6, 6
	s_ashr_i32 s4, s8, 3
	s_cbranch_execz .LBB0_496
	s_branch .LBB0_497
